# write-through (sc0 sc1) stores in the w_in and w_out GEMM epilogues so the grid barrier's L2 writeback has less dirty data
# baseline (speedup 1.0000x reference)
.LBB0_169:
	s_add_u32 s42, s40, 0xfff80080
	s_addc_u32 s43, s41, -1
	s_add_i32 s62, 0, 0x10000
	v_add_u32_e32 v140, s62, v143
	ds_read_b128 v[146:149], v140
	ds_read_b128 v[150:153], v140 offset:1024
	ds_read_b128 v[154:157], v140 offset:2048
	ds_read_b128 v[158:161], v140 offset:3072
	s_cmp_eq_u32 s61, 28
	s_cselect_b32 s51, s11, s43
	s_cselect_b32 s50, s52, s42
	s_cselect_b32 s43, s1, s60
	s_cselect_b32 s42, s53, s58
	v_lshl_add_u64 v[140:141], s[40:41], 0, v[136:137]
	s_add_i32 m0, s26, 0xc000
	ds_read_b128 v[162:165], v145
	ds_read_b128 v[166:169], v145 offset:1024
	ds_read_b128 v[170:173], v145 offset:2048
	ds_read_b128 v[174:177], v145 offset:3072
	ds_read_b128 v[178:181], v145 offset:4096
	ds_read_b128 v[182:185], v145 offset:5120
	ds_read_b128 v[186:189], v145 offset:6144
	ds_read_b128 v[190:193], v145 offset:7168
	global_load_lds_dwordx4 v[140:141], off
	v_lshl_add_u64 v[140:141], s[40:41], 0, v[138:139]
	s_add_i32 m0, s26, 0xe000
	s_nop 0
	global_load_lds_dwordx4 v[140:141], off
	s_waitcnt lgkmcnt(8)
	s_barrier
	s_waitcnt lgkmcnt(0)
	s_setprio 1
	s_waitcnt lgkmcnt(0)
	v_mfma_f32_16x16x32_bf16 v[126:129], v[146:149], v[162:165], v[126:129]
	v_mfma_f32_16x16x32_bf16 v[122:125], v[154:157], v[162:165], v[122:125]
	v_mfma_f32_16x16x32_bf16 v[114:117], v[146:149], v[170:173], v[114:117]
	v_mfma_f32_16x16x32_bf16 v[106:109], v[154:157], v[170:173], v[106:109]
	v_mfma_f32_16x16x32_bf16 v[98:101], v[146:149], v[178:181], v[98:101]
	v_mfma_f32_16x16x32_bf16 v[90:93], v[154:157], v[178:181], v[90:93]
	v_mfma_f32_16x16x32_bf16 v[82:85], v[146:149], v[186:189], v[82:85]
	v_mfma_f32_16x16x32_bf16 v[74:77], v[154:157], v[186:189], v[74:77]
	v_mfma_f32_16x16x32_bf16 v[126:129], v[150:153], v[166:169], v[126:129]
	v_mfma_f32_16x16x32_bf16 v[122:125], v[158:161], v[166:169], v[122:125]
	v_mfma_f32_16x16x32_bf16 v[114:117], v[150:153], v[174:177], v[114:117]
	v_mfma_f32_16x16x32_bf16 v[106:109], v[158:161], v[174:177], v[106:109]
	v_mfma_f32_16x16x32_bf16 v[98:101], v[150:153], v[182:185], v[98:101]
	v_mfma_f32_16x16x32_bf16 v[90:93], v[158:161], v[182:185], v[90:93]
	v_mfma_f32_16x16x32_bf16 v[82:85], v[150:153], v[190:193], v[82:85]
	v_mfma_f32_16x16x32_bf16 v[74:77], v[158:161], v[190:193], v[74:77]
	s_setprio 0
	s_barrier
	s_add_i32 s64, 0, 0x14000
	v_add_u32_e32 v140, s64, v143
	s_add_i32 s62, s62, s7
	ds_read_b128 v[194:197], v140
	ds_read_b128 v[198:201], v140 offset:1024
	ds_read_b128 v[202:205], v140 offset:2048
	ds_read_b128 v[234:237], v140 offset:3072
	v_lshl_add_u64 v[140:141], s[42:43], 0, v[210:211]
	s_mov_b32 m0, s62
	v_lshl_add_u64 v[218:219], s[42:43], 0, v[130:131]
	global_load_lds_dwordx4 v[140:141], off
	s_add_i32 m0, s62, 0x2000
	s_nop 0
	global_load_lds_dwordx4 v[218:219], off
	s_barrier
	s_waitcnt lgkmcnt(0)
	s_setprio 1
	s_waitcnt lgkmcnt(0)
	v_mfma_f32_16x16x32_bf16 v[118:121], v[194:197], v[162:165], v[118:121]
	v_mfma_f32_16x16x32_bf16 v[110:113], v[202:205], v[162:165], v[110:113]
	v_mfma_f32_16x16x32_bf16 v[102:105], v[194:197], v[170:173], v[102:105]
	v_mfma_f32_16x16x32_bf16 v[94:97], v[202:205], v[170:173], v[94:97]
	v_mfma_f32_16x16x32_bf16 v[86:89], v[194:197], v[178:181], v[86:89]
	v_mfma_f32_16x16x32_bf16 v[78:81], v[202:205], v[178:181], v[78:81]
	v_mfma_f32_16x16x32_bf16 v[70:73], v[194:197], v[186:189], v[70:73]
	v_mfma_f32_16x16x32_bf16 v[66:69], v[202:205], v[186:189], v[66:69]
	v_mfma_f32_16x16x32_bf16 v[118:121], v[198:201], v[166:169], v[118:121]
	v_mfma_f32_16x16x32_bf16 v[110:113], v[234:237], v[166:169], v[110:113]
	v_mfma_f32_16x16x32_bf16 v[102:105], v[198:201], v[174:177], v[102:105]
	v_mfma_f32_16x16x32_bf16 v[94:97], v[234:237], v[174:177], v[94:97]
	v_mfma_f32_16x16x32_bf16 v[86:89], v[198:201], v[182:185], v[86:89]
	v_mfma_f32_16x16x32_bf16 v[78:81], v[234:237], v[182:185], v[78:81]
	v_mfma_f32_16x16x32_bf16 v[70:73], v[198:201], v[190:193], v[70:73]
	v_mfma_f32_16x16x32_bf16 v[66:69], v[234:237], v[190:193], v[66:69]
	s_setprio 0
	s_mov_b32 m0, s26
	v_lshl_add_u64 v[238:239], s[50:51], 0, v[134:135]
	s_barrier
	ds_read_b128 v[162:165], v145 offset:16384
	ds_read_b128 v[166:169], v145 offset:17408
	ds_read_b128 v[170:173], v145 offset:18432
	ds_read_b128 v[174:177], v145 offset:19456
	ds_read_b128 v[178:181], v145 offset:20480
	ds_read_b128 v[182:185], v145 offset:21504
	ds_read_b128 v[186:189], v145 offset:22528
	ds_read_b128 v[190:193], v145 offset:23552
	global_load_lds_dwordx4 v[238:239], off
	v_lshl_add_u64 v[240:241], s[50:51], 0, v[132:133]
	s_mov_b32 m0, s27
	s_nop 0
	global_load_lds_dwordx4 v[240:241], off
	s_barrier
	s_waitcnt lgkmcnt(0)
	s_setprio 1
	s_waitcnt lgkmcnt(0)
	v_mfma_f32_16x16x32_bf16 v[62:65], v[146:149], v[162:165], v[62:65]
	v_mfma_f32_16x16x32_bf16 v[58:61], v[154:157], v[162:165], v[58:61]
	v_mfma_f32_16x16x32_bf16 v[50:53], v[146:149], v[170:173], v[50:53]
	v_mfma_f32_16x16x32_bf16 v[42:45], v[154:157], v[170:173], v[42:45]
	v_mfma_f32_16x16x32_bf16 v[34:37], v[146:149], v[178:181], v[34:37]
	v_mfma_f32_16x16x32_bf16 v[26:29], v[154:157], v[178:181], v[26:29]
	v_mfma_f32_16x16x32_bf16 v[18:21], v[146:149], v[186:189], v[18:21]
	v_mfma_f32_16x16x32_bf16 v[10:13], v[154:157], v[186:189], v[10:13]
	v_mfma_f32_16x16x32_bf16 v[62:65], v[150:153], v[166:169], v[62:65]
	v_mfma_f32_16x16x32_bf16 v[58:61], v[158:161], v[166:169], v[58:61]
	v_mfma_f32_16x16x32_bf16 v[50:53], v[150:153], v[174:177], v[50:53]
	v_mfma_f32_16x16x32_bf16 v[42:45], v[158:161], v[174:177], v[42:45]
	v_mfma_f32_16x16x32_bf16 v[34:37], v[150:153], v[182:185], v[34:37]
	v_mfma_f32_16x16x32_bf16 v[26:29], v[158:161], v[182:185], v[26:29]
	v_mfma_f32_16x16x32_bf16 v[18:21], v[150:153], v[190:193], v[18:21]
	v_mfma_f32_16x16x32_bf16 v[10:13], v[158:161], v[190:193], v[10:13]
	s_setprio 0
	s_barrier
	s_add_u32 s62, s42, 0x80000
	s_addc_u32 s63, s43, 0
	s_add_i32 s64, s64, s7
	v_lshl_add_u64 v[146:147], s[62:63], 0, v[210:211]
	s_mov_b32 m0, s64
	s_nop 0
	global_load_lds_dwordx4 v[146:147], off
	v_lshl_add_u64 v[146:147], s[62:63], 0, v[130:131]
	s_add_i32 m0, s64, 0x2000
	s_nop 0
	global_load_lds_dwordx4 v[146:147], off
	s_waitcnt vmcnt(6)
	s_barrier
	s_setprio 1
	v_mfma_f32_16x16x32_bf16 v[54:57], v[194:197], v[162:165], v[54:57]
	v_mfma_f32_16x16x32_bf16 v[46:49], v[202:205], v[162:165], v[46:49]
	v_mfma_f32_16x16x32_bf16 v[38:41], v[194:197], v[170:173], v[38:41]
	v_mfma_f32_16x16x32_bf16 v[30:33], v[202:205], v[170:173], v[30:33]
	v_mfma_f32_16x16x32_bf16 v[22:25], v[194:197], v[178:181], v[22:25]
	v_mfma_f32_16x16x32_bf16 v[14:17], v[202:205], v[178:181], v[14:17]
	v_mfma_f32_16x16x32_bf16 v[6:9], v[194:197], v[186:189], v[6:9]
	v_mfma_f32_16x16x32_bf16 v[2:5], v[202:205], v[186:189], v[2:5]
	v_mfma_f32_16x16x32_bf16 v[54:57], v[198:201], v[166:169], v[54:57]
	v_mfma_f32_16x16x32_bf16 v[46:49], v[234:237], v[166:169], v[46:49]
	v_mfma_f32_16x16x32_bf16 v[38:41], v[198:201], v[174:177], v[38:41]
	v_mfma_f32_16x16x32_bf16 v[30:33], v[234:237], v[174:177], v[30:33]
	v_mfma_f32_16x16x32_bf16 v[22:25], v[198:201], v[182:185], v[22:25]
	v_mfma_f32_16x16x32_bf16 v[14:17], v[234:237], v[182:185], v[14:17]
	v_mfma_f32_16x16x32_bf16 v[6:9], v[198:201], v[190:193], v[6:9]
	v_mfma_f32_16x16x32_bf16 v[2:5], v[234:237], v[190:193], v[2:5]
	s_setprio 0
	s_add_i32 s62, 0, 0x18000
	v_add_u32_e32 v158, s62, v143
	s_barrier
	ds_read_b128 v[146:149], v158
	ds_read_b128 v[150:153], v158 offset:1024
	ds_read_b128 v[154:157], v158 offset:2048
	ds_read_b128 v[158:161], v158 offset:3072
	s_add_u32 s50, s50, 0x80000
	s_addc_u32 s51, s51, 0
	s_mov_b32 m0, s28
	v_lshl_add_u64 v[194:195], s[50:51], 0, v[134:135]
	ds_read_b128 v[162:165], v145 offset:32768
	ds_read_b128 v[166:169], v145 offset:33792
	ds_read_b128 v[170:173], v145 offset:34816
	ds_read_b128 v[174:177], v145 offset:35840
	ds_read_b128 v[178:181], v145 offset:36864
	ds_read_b128 v[182:185], v145 offset:37888
	ds_read_b128 v[186:189], v145 offset:38912
	ds_read_b128 v[190:193], v145 offset:39936
	global_load_lds_dwordx4 v[194:195], off
	v_lshl_add_u64 v[194:195], s[50:51], 0, v[132:133]
	s_mov_b32 m0, s29
	s_nop 0
	global_load_lds_dwordx4 v[194:195], off
	s_waitcnt lgkmcnt(8)
	s_barrier
	s_waitcnt lgkmcnt(0)
	s_setprio 1
	s_waitcnt lgkmcnt(0)
	v_mfma_f32_16x16x32_bf16 v[126:129], v[146:149], v[162:165], v[126:129]
	v_mfma_f32_16x16x32_bf16 v[122:125], v[154:157], v[162:165], v[122:125]
	v_mfma_f32_16x16x32_bf16 v[114:117], v[146:149], v[170:173], v[114:117]
	v_mfma_f32_16x16x32_bf16 v[106:109], v[154:157], v[170:173], v[106:109]
	v_mfma_f32_16x16x32_bf16 v[98:101], v[146:149], v[178:181], v[98:101]
	v_mfma_f32_16x16x32_bf16 v[90:93], v[154:157], v[178:181], v[90:93]
	v_mfma_f32_16x16x32_bf16 v[82:85], v[146:149], v[186:189], v[82:85]
	v_mfma_f32_16x16x32_bf16 v[74:77], v[154:157], v[186:189], v[74:77]
	v_mfma_f32_16x16x32_bf16 v[126:129], v[150:153], v[166:169], v[126:129]
	v_mfma_f32_16x16x32_bf16 v[122:125], v[158:161], v[166:169], v[122:125]
	v_mfma_f32_16x16x32_bf16 v[114:117], v[150:153], v[174:177], v[114:117]
	v_mfma_f32_16x16x32_bf16 v[106:109], v[158:161], v[174:177], v[106:109]
	v_mfma_f32_16x16x32_bf16 v[98:101], v[150:153], v[182:185], v[98:101]
	v_mfma_f32_16x16x32_bf16 v[90:93], v[158:161], v[182:185], v[90:93]
	v_mfma_f32_16x16x32_bf16 v[82:85], v[150:153], v[190:193], v[82:85]
	v_mfma_f32_16x16x32_bf16 v[74:77], v[158:161], v[190:193], v[74:77]
	s_setprio 0
	s_barrier
	s_add_i32 s50, 0, 0x1c000
	s_add_i32 s51, s62, s7
	v_add_u32_e32 v226, s50, v143
	v_lshl_add_u64 v[140:141], v[140:141], 0, s[36:37]
	s_mov_b32 m0, s51
	ds_read_b128 v[194:197], v226
	ds_read_b128 v[198:201], v226 offset:1024
	ds_read_b128 v[202:205], v226 offset:2048
	ds_read_b128 v[234:237], v226 offset:3072
	global_load_lds_dwordx4 v[140:141], off
	v_lshl_add_u64 v[140:141], v[218:219], 0, s[36:37]
	s_add_i32 m0, s51, 0x2000
	s_nop 0
	global_load_lds_dwordx4 v[140:141], off
	s_barrier
	s_waitcnt lgkmcnt(0)
	s_setprio 1
	s_waitcnt lgkmcnt(0)
	v_mfma_f32_16x16x32_bf16 v[118:121], v[194:197], v[162:165], v[118:121]
	v_mfma_f32_16x16x32_bf16 v[110:113], v[202:205], v[162:165], v[110:113]
	v_mfma_f32_16x16x32_bf16 v[102:105], v[194:197], v[170:173], v[102:105]
	v_mfma_f32_16x16x32_bf16 v[94:97], v[202:205], v[170:173], v[94:97]
	v_mfma_f32_16x16x32_bf16 v[86:89], v[194:197], v[178:181], v[86:89]
	v_mfma_f32_16x16x32_bf16 v[78:81], v[202:205], v[178:181], v[78:81]
	v_mfma_f32_16x16x32_bf16 v[70:73], v[194:197], v[186:189], v[70:73]
	v_mfma_f32_16x16x32_bf16 v[66:69], v[202:205], v[186:189], v[66:69]
	v_mfma_f32_16x16x32_bf16 v[118:121], v[198:201], v[166:169], v[118:121]
	v_mfma_f32_16x16x32_bf16 v[110:113], v[234:237], v[166:169], v[110:113]
	v_mfma_f32_16x16x32_bf16 v[102:105], v[198:201], v[174:177], v[102:105]
	v_mfma_f32_16x16x32_bf16 v[94:97], v[234:237], v[174:177], v[94:97]
	v_mfma_f32_16x16x32_bf16 v[86:89], v[198:201], v[182:185], v[86:89]
	v_mfma_f32_16x16x32_bf16 v[78:81], v[234:237], v[182:185], v[78:81]
	v_mfma_f32_16x16x32_bf16 v[70:73], v[198:201], v[190:193], v[70:73]
	v_mfma_f32_16x16x32_bf16 v[66:69], v[234:237], v[190:193], v[66:69]
	s_setprio 0
	s_mov_b32 m0, s33
	v_lshl_add_u64 v[140:141], v[238:239], 0, s[36:37]
	s_barrier
	ds_read_b128 v[162:165], v145 offset:49152
	ds_read_b128 v[166:169], v145 offset:50176
	ds_read_b128 v[170:173], v145 offset:51200
	ds_read_b128 v[174:177], v145 offset:52224
	ds_read_b128 v[178:181], v145 offset:53248
	ds_read_b128 v[182:185], v145 offset:54272
	ds_read_b128 v[186:189], v145 offset:55296
	ds_read_b128 v[190:193], v145 offset:56320
	global_load_lds_dwordx4 v[140:141], off
	v_lshl_add_u64 v[140:141], v[240:241], 0, s[36:37]
	s_mov_b32 m0, s46
	s_nop 0
	global_load_lds_dwordx4 v[140:141], off
	s_barrier
	s_waitcnt lgkmcnt(0)
	s_setprio 1
	s_waitcnt lgkmcnt(0)
	v_mfma_f32_16x16x32_bf16 v[62:65], v[146:149], v[162:165], v[62:65]
	v_mfma_f32_16x16x32_bf16 v[58:61], v[154:157], v[162:165], v[58:61]
	v_mfma_f32_16x16x32_bf16 v[50:53], v[146:149], v[170:173], v[50:53]
	v_mfma_f32_16x16x32_bf16 v[42:45], v[154:157], v[170:173], v[42:45]
	v_mfma_f32_16x16x32_bf16 v[34:37], v[146:149], v[178:181], v[34:37]
	v_mfma_f32_16x16x32_bf16 v[26:29], v[154:157], v[178:181], v[26:29]
	v_mfma_f32_16x16x32_bf16 v[18:21], v[146:149], v[186:189], v[18:21]
	v_mfma_f32_16x16x32_bf16 v[10:13], v[154:157], v[186:189], v[10:13]
	v_mfma_f32_16x16x32_bf16 v[62:65], v[150:153], v[166:169], v[62:65]
	v_mfma_f32_16x16x32_bf16 v[58:61], v[158:161], v[166:169], v[58:61]
	v_mfma_f32_16x16x32_bf16 v[50:53], v[150:153], v[174:177], v[50:53]
	v_mfma_f32_16x16x32_bf16 v[42:45], v[158:161], v[174:177], v[42:45]
	v_mfma_f32_16x16x32_bf16 v[34:37], v[150:153], v[182:185], v[34:37]
	v_mfma_f32_16x16x32_bf16 v[26:29], v[158:161], v[182:185], v[26:29]
	v_mfma_f32_16x16x32_bf16 v[18:21], v[150:153], v[190:193], v[18:21]
	v_mfma_f32_16x16x32_bf16 v[10:13], v[158:161], v[190:193], v[10:13]
	s_setprio 0
	s_barrier
	s_add_u32 s42, s42, 0x80080
	s_addc_u32 s43, s43, 0
	s_add_i32 s50, s50, s7
	v_lshl_add_u64 v[140:141], s[42:43], 0, v[210:211]
	s_mov_b32 m0, s50
	s_nop 0
	global_load_lds_dwordx4 v[140:141], off
	v_lshl_add_u64 v[140:141], s[42:43], 0, v[130:131]
	s_add_i32 m0, s50, 0x2000
	s_nop 0
	global_load_lds_dwordx4 v[140:141], off
	s_waitcnt vmcnt(6)
	s_barrier
	s_setprio 1
	v_mfma_f32_16x16x32_bf16 v[54:57], v[194:197], v[162:165], v[54:57]
	v_mfma_f32_16x16x32_bf16 v[46:49], v[202:205], v[162:165], v[46:49]
	v_mfma_f32_16x16x32_bf16 v[38:41], v[194:197], v[170:173], v[38:41]
	v_mfma_f32_16x16x32_bf16 v[30:33], v[202:205], v[170:173], v[30:33]
	v_mfma_f32_16x16x32_bf16 v[22:25], v[194:197], v[178:181], v[22:25]
	v_mfma_f32_16x16x32_bf16 v[14:17], v[202:205], v[178:181], v[14:17]
	v_mfma_f32_16x16x32_bf16 v[6:9], v[194:197], v[186:189], v[6:9]
	v_mfma_f32_16x16x32_bf16 v[2:5], v[202:205], v[186:189], v[2:5]
	v_mfma_f32_16x16x32_bf16 v[54:57], v[198:201], v[166:169], v[54:57]
	v_mfma_f32_16x16x32_bf16 v[46:49], v[234:237], v[166:169], v[46:49]
	v_mfma_f32_16x16x32_bf16 v[38:41], v[198:201], v[174:177], v[38:41]
	v_mfma_f32_16x16x32_bf16 v[30:33], v[234:237], v[174:177], v[30:33]
	v_mfma_f32_16x16x32_bf16 v[22:25], v[198:201], v[182:185], v[22:25]
	v_mfma_f32_16x16x32_bf16 v[14:17], v[234:237], v[182:185], v[14:17]
	v_mfma_f32_16x16x32_bf16 v[6:9], v[198:201], v[190:193], v[6:9]
	v_mfma_f32_16x16x32_bf16 v[2:5], v[234:237], v[190:193], v[2:5]
	s_setprio 0
	s_add_i32 s61, s61, 2
	s_add_u32 s40, s40, 0x100
	s_addc_u32 s41, s41, 0
	s_add_u32 s58, s58, 0x100
	s_addc_u32 s60, s60, 0
	s_cmp_gt_u32 s61, 29
	s_barrier
	s_cbranch_scc0 .LBB0_169
	v_lshl_or_b32 v140, s4, 8, v144
	v_ashrrev_i32_e32 v141, 31, v140
	v_lshl_add_u32 v150, s5, 8, v142
	v_lshl_add_u64 v[140:141], v[140:141], 1, s[8:9]
	s_movk_i32 s58, 0x2c00
	v_mad_i64_i32 v[146:147], s[4:5], v150, s58, v[140:141]
	v_pk_add_f32 v[128:129], v[128:129], 0 op_sel_hi:[1,0]
	v_pk_add_f32 v[126:127], v[126:127], 0 op_sel_hi:[1,0]
	v_pk_add_f32 v[148:149], v[124:125], 0 op_sel_hi:[1,0]
	v_pk_add_f32 v[124:125], v[122:123], 0 op_sel_hi:[1,0]
	v_cvt_pk_bf16_f32 v122, v126, v127
	v_cvt_pk_bf16_f32 v123, v128, v129
	v_pk_add_f32 v[118:119], v[118:119], 0 op_sel_hi:[1,0]
	v_cvt_pk_bf16_f32 v124, v124, v125
	v_cvt_pk_bf16_f32 v125, v148, v149
	global_store_dwordx4 v[146:147], v[122:125], off sc0 sc1
	v_pk_add_f32 v[120:121], v[120:121], 0 op_sel_hi:[1,0]
	v_pk_add_f32 v[114:115], v[114:115], 0 op_sel_hi:[1,0]
	v_pk_add_f32 v[122:123], v[112:113], 0 op_sel_hi:[1,0]
	v_pk_add_f32 v[112:113], v[110:111], 0 op_sel_hi:[1,0]
	v_cvt_pk_bf16_f32 v110, v118, v119
	v_cvt_pk_bf16_f32 v111, v120, v121
	v_pk_add_f32 v[102:103], v[102:103], 0 op_sel_hi:[1,0]
	v_cvt_pk_bf16_f32 v112, v112, v113
	v_cvt_pk_bf16_f32 v113, v122, v123
	global_store_dwordx4 v[146:147], v[110:113], off offset:256 sc0 sc1
	v_pk_add_f32 v[104:105], v[104:105], 0 op_sel_hi:[1,0]
	v_pk_add_f32 v[98:99], v[98:99], 0 op_sel_hi:[1,0]
	v_or_b32_e32 v110, 16, v150
	v_mad_i64_i32 v[110:111], s[4:5], v110, s58, v[140:141]
	v_pk_add_f32 v[112:113], v[116:117], 0 op_sel_hi:[1,0]
	v_pk_add_f32 v[116:117], v[108:109], 0 op_sel_hi:[1,0]
	v_pk_add_f32 v[108:109], v[106:107], 0 op_sel_hi:[1,0]
	v_cvt_pk_bf16_f32 v106, v114, v115
	v_cvt_pk_bf16_f32 v107, v112, v113
	v_pk_add_f32 v[86:87], v[86:87], 0 op_sel_hi:[1,0]
	v_cvt_pk_bf16_f32 v108, v108, v109
	v_cvt_pk_bf16_f32 v109, v116, v117
	global_store_dwordx4 v[110:111], v[106:109], off sc0 sc1
	v_pk_add_f32 v[88:89], v[88:89], 0 op_sel_hi:[1,0]
	v_pk_add_f32 v[82:83], v[82:83], 0 op_sel_hi:[1,0]
	v_pk_add_f32 v[106:107], v[96:97], 0 op_sel_hi:[1,0]
	v_pk_add_f32 v[96:97], v[94:95], 0 op_sel_hi:[1,0]
	v_cvt_pk_bf16_f32 v94, v102, v103
	v_cvt_pk_bf16_f32 v95, v104, v105
	v_pk_add_f32 v[70:71], v[70:71], 0 op_sel_hi:[1,0]
	v_cvt_pk_bf16_f32 v96, v96, v97
	v_cvt_pk_bf16_f32 v97, v106, v107
	global_store_dwordx4 v[110:111], v[94:97], off offset:256 sc0 sc1
	v_pk_add_f32 v[72:73], v[72:73], 0 op_sel_hi:[1,0]
	v_pk_add_f32 v[64:65], v[64:65], 0 op_sel_hi:[1,0]
	v_or_b32_e32 v94, 32, v150
	v_mad_i64_i32 v[94:95], s[4:5], v94, s58, v[140:141]
	v_pk_add_f32 v[96:97], v[100:101], 0 op_sel_hi:[1,0]
	v_pk_add_f32 v[100:101], v[92:93], 0 op_sel_hi:[1,0]
	v_pk_add_f32 v[92:93], v[90:91], 0 op_sel_hi:[1,0]
	v_cvt_pk_bf16_f32 v90, v98, v99
	v_cvt_pk_bf16_f32 v91, v96, v97
	v_pk_add_f32 v[62:63], v[62:63], 0 op_sel_hi:[1,0]
	v_cvt_pk_bf16_f32 v92, v92, v93
	v_cvt_pk_bf16_f32 v93, v100, v101
	global_store_dwordx4 v[94:95], v[90:93], off sc0 sc1
	v_pk_add_f32 v[54:55], v[54:55], 0 op_sel_hi:[1,0]
	v_pk_add_f32 v[56:57], v[56:57], 0 op_sel_hi:[1,0]
	v_pk_add_f32 v[90:91], v[80:81], 0 op_sel_hi:[1,0]
	v_pk_add_f32 v[80:81], v[78:79], 0 op_sel_hi:[1,0]
	v_cvt_pk_bf16_f32 v78, v86, v87
	v_cvt_pk_bf16_f32 v79, v88, v89
	v_pk_add_f32 v[50:51], v[50:51], 0 op_sel_hi:[1,0]
	v_cvt_pk_bf16_f32 v80, v80, v81
	v_cvt_pk_bf16_f32 v81, v90, v91
	global_store_dwordx4 v[94:95], v[78:81], off offset:256 sc0 sc1
	v_pk_add_f32 v[38:39], v[38:39], 0 op_sel_hi:[1,0]
	v_pk_add_f32 v[40:41], v[40:41], 0 op_sel_hi:[1,0]
	v_or_b32_e32 v78, 48, v150
	v_mad_i64_i32 v[78:79], s[4:5], v78, s58, v[140:141]
	v_pk_add_f32 v[80:81], v[84:85], 0 op_sel_hi:[1,0]
	v_pk_add_f32 v[84:85], v[76:77], 0 op_sel_hi:[1,0]
	v_pk_add_f32 v[76:77], v[74:75], 0 op_sel_hi:[1,0]
	v_cvt_pk_bf16_f32 v74, v82, v83
	v_cvt_pk_bf16_f32 v75, v80, v81
	v_pk_add_f32 v[34:35], v[34:35], 0 op_sel_hi:[1,0]
	v_cvt_pk_bf16_f32 v76, v76, v77
	v_cvt_pk_bf16_f32 v77, v84, v85
	global_store_dwordx4 v[78:79], v[74:77], off sc0 sc1
	v_pk_add_f32 v[22:23], v[22:23], 0 op_sel_hi:[1,0]
	v_pk_add_f32 v[24:25], v[24:25], 0 op_sel_hi:[1,0]
	v_pk_add_f32 v[74:75], v[68:69], 0 op_sel_hi:[1,0]
	v_pk_add_f32 v[68:69], v[66:67], 0 op_sel_hi:[1,0]
	v_cvt_pk_bf16_f32 v66, v70, v71
	v_cvt_pk_bf16_f32 v67, v72, v73
	v_pk_add_f32 v[18:19], v[18:19], 0 op_sel_hi:[1,0]
	v_cvt_pk_bf16_f32 v68, v68, v69
	v_cvt_pk_bf16_f32 v69, v74, v75
	global_store_dwordx4 v[78:79], v[66:69], off offset:256 sc0 sc1
	v_readlane_b32 s64, v255, 43
	v_readlane_b32 s60, v255, 45
	v_add_u32_e32 v66, 0x80, v150
	v_mad_i64_i32 v[66:67], s[4:5], v66, s58, v[140:141]
	v_pk_add_f32 v[68:69], v[60:61], 0 op_sel_hi:[1,0]
	v_pk_add_f32 v[60:61], v[58:59], 0 op_sel_hi:[1,0]
	v_cvt_pk_bf16_f32 v58, v62, v63
	v_cvt_pk_bf16_f32 v59, v64, v65
	s_and_b64 vcc, exec, s[38:39]
	v_cvt_pk_bf16_f32 v60, v60, v61
	v_cvt_pk_bf16_f32 v61, v68, v69
	global_store_dwordx4 v[66:67], v[58:61], off sc0 sc1
	s_mov_b64 s[42:43], s[34:35]
	s_mov_b64 s[40:41], s[24:25]
	v_pk_add_f32 v[58:59], v[48:49], 0 op_sel_hi:[1,0]
	v_pk_add_f32 v[48:49], v[46:47], 0 op_sel_hi:[1,0]
	v_cvt_pk_bf16_f32 v46, v54, v55
	v_cvt_pk_bf16_f32 v47, v56, v57
	v_readlane_b32 s65, v255, 44
	v_cvt_pk_bf16_f32 v48, v48, v49
	v_cvt_pk_bf16_f32 v49, v58, v59
	global_store_dwordx4 v[66:67], v[46:49], off offset:256 sc0 sc1
	v_readlane_b32 s61, v255, 46
	v_pk_add_f32 v[8:9], v[8:9], 0 op_sel_hi:[1,0]
	v_add_u32_e32 v46, 0x90, v150
	v_mad_i64_i32 v[46:47], s[4:5], v46, s58, v[140:141]
	v_pk_add_f32 v[48:49], v[52:53], 0 op_sel_hi:[1,0]
	v_pk_add_f32 v[52:53], v[44:45], 0 op_sel_hi:[1,0]
	v_pk_add_f32 v[44:45], v[42:43], 0 op_sel_hi:[1,0]
	v_cvt_pk_bf16_f32 v42, v50, v51
	v_cvt_pk_bf16_f32 v43, v48, v49
	v_pk_add_f32 v[6:7], v[6:7], 0 op_sel_hi:[1,0]
	v_cvt_pk_bf16_f32 v44, v44, v45
	v_cvt_pk_bf16_f32 v45, v52, v53
	global_store_dwordx4 v[46:47], v[42:45], off sc0 sc1
	s_nop 1
	v_pk_add_f32 v[42:43], v[32:33], 0 op_sel_hi:[1,0]
	v_pk_add_f32 v[32:33], v[30:31], 0 op_sel_hi:[1,0]
	v_cvt_pk_bf16_f32 v30, v38, v39
	v_cvt_pk_bf16_f32 v31, v40, v41
	s_nop 0
	v_cvt_pk_bf16_f32 v32, v32, v33
	v_cvt_pk_bf16_f32 v33, v42, v43
	global_store_dwordx4 v[46:47], v[30:33], off offset:256 sc0 sc1
	s_nop 1
	v_add_u32_e32 v30, 0xa0, v150
	v_mad_i64_i32 v[30:31], s[4:5], v30, s58, v[140:141]
	v_pk_add_f32 v[32:33], v[36:37], 0 op_sel_hi:[1,0]
	v_pk_add_f32 v[36:37], v[28:29], 0 op_sel_hi:[1,0]
	v_pk_add_f32 v[28:29], v[26:27], 0 op_sel_hi:[1,0]
	v_cvt_pk_bf16_f32 v26, v34, v35
	v_cvt_pk_bf16_f32 v27, v32, v33
	s_nop 0
	v_cvt_pk_bf16_f32 v28, v28, v29
	v_cvt_pk_bf16_f32 v29, v36, v37
	global_store_dwordx4 v[30:31], v[26:29], off sc0 sc1
	s_nop 1
	v_pk_add_f32 v[26:27], v[16:17], 0 op_sel_hi:[1,0]
	v_pk_add_f32 v[16:17], v[14:15], 0 op_sel_hi:[1,0]
	v_cvt_pk_bf16_f32 v14, v22, v23
	v_cvt_pk_bf16_f32 v15, v24, v25
	s_nop 0
	v_cvt_pk_bf16_f32 v16, v16, v17
	v_cvt_pk_bf16_f32 v17, v26, v27
	global_store_dwordx4 v[30:31], v[14:17], off offset:256 sc0 sc1
	s_nop 1
	v_add_u32_e32 v14, 0xb0, v150
	v_mad_i64_i32 v[14:15], s[4:5], v14, s58, v[140:141]
	v_pk_add_f32 v[16:17], v[20:21], 0 op_sel_hi:[1,0]
	v_pk_add_f32 v[20:21], v[12:13], 0 op_sel_hi:[1,0]
	v_pk_add_f32 v[12:13], v[10:11], 0 op_sel_hi:[1,0]
	v_cvt_pk_bf16_f32 v10, v18, v19
	v_cvt_pk_bf16_f32 v11, v16, v17
	s_mov_b32 s4, s0
	v_cvt_pk_bf16_f32 v12, v12, v13
	v_cvt_pk_bf16_f32 v13, v20, v21
	global_store_dwordx4 v[14:15], v[10:13], off sc0 sc1
	s_mov_b32 s5, s10
	s_nop 0
	v_pk_add_f32 v[10:11], v[4:5], 0 op_sel_hi:[1,0]
	v_pk_add_f32 v[4:5], v[2:3], 0 op_sel_hi:[1,0]
	v_cvt_pk_bf16_f32 v2, v6, v7
	v_cvt_pk_bf16_f32 v3, v8, v9
	s_nop 0
	v_cvt_pk_bf16_f32 v4, v4, v5
	v_cvt_pk_bf16_f32 v5, v10, v11
	global_store_dwordx4 v[14:15], v[2:5], off offset:256 sc0 sc1
	s_cbranch_vccz .LBB0_162
	s_waitcnt vmcnt(0)
	v_readlane_b32 s46, v255, 41
	s_cmpk_gt_u32 s2, 0xff
	v_readlane_b32 s47, v255, 42
	s_cbranch_scc1 .LBB0_173
	s_barrier

.LBB0_477:
	v_lshl_or_b32 v168, s34, 8, v171
	v_ashrrev_i32_e32 v169, 31, v168
	v_lshl_add_u64 v[130:131], v[168:169], 2, s[62:63]
	global_load_dwordx4 v[142:145], v[130:131], off
	global_load_dwordx4 v[138:141], v[130:131], off offset:64
	global_load_dwordx4 v[134:137], v[130:131], off offset:512
	s_nop 0
	global_load_dwordx4 v[130:133], v[130:131], off offset:576
	v_lshl_add_u64 v[250:251], v[148:149], 0, v[168:169]
	v_lshlrev_b64 v[250:251], 2, v[250:251]
	v_lshl_add_u64 v[218:219], s[0:1], 0, v[250:251]
	global_load_dwordx4 v[174:177], v[218:219], off
	global_load_dwordx4 v[178:181], v[218:219], off offset:64
	global_load_dwordx4 v[182:185], v[218:219], off offset:512
	global_load_dwordx4 v[186:189], v[218:219], off offset:576
	v_lshl_add_u64 v[250:251], v[150:151], 0, v[168:169]
	v_lshlrev_b64 v[250:251], 2, v[250:251]
	v_lshl_add_u64 v[218:219], s[0:1], 0, v[250:251]
	global_load_dwordx4 v[190:193], v[218:219], off
	global_load_dwordx4 v[194:197], v[218:219], off offset:64
	global_load_dwordx4 v[198:201], v[218:219], off offset:512
	global_load_dwordx4 v[202:205], v[218:219], off offset:576
	v_lshl_add_u64 v[250:251], v[152:153], 0, v[168:169]
	v_lshlrev_b64 v[250:251], 2, v[250:251]
	v_lshl_add_u64 v[218:219], s[0:1], 0, v[250:251]
	global_load_dwordx4 v[234:237], v[218:219], off
	global_load_dwordx4 v[238:241], v[218:219], off offset:64
	global_load_dwordx4 v[242:245], v[218:219], off offset:512
	global_load_dwordx4 v[246:249], v[218:219], off offset:576
	s_and_b64 vcc, exec, s[38:39]
	s_mov_b32 s34, s24
	s_mov_b32 s74, s40
	s_mov_b64 s[76:77], s[42:43]
	s_waitcnt vmcnt(8)
	v_lshl_add_u64 v[250:251], v[148:149], 0, v[168:169]
	v_lshlrev_b64 v[250:251], 2, v[250:251]
	v_lshl_add_u64 v[226:227], s[50:51], 0, v[250:251]
	v_pk_fma_f32 v[128:129], v[128:129], v[144:145], v[176:177]
	v_pk_fma_f32 v[126:127], v[126:127], v[142:143], v[174:175]
	v_pk_fma_f32 v[124:125], v[124:125], v[140:141], v[180:181]
	v_pk_fma_f32 v[122:123], v[122:123], v[138:139], v[178:179]
	v_pk_fma_f32 v[120:121], v[120:121], v[136:137], v[184:185]
	v_pk_fma_f32 v[118:119], v[118:119], v[134:135], v[182:183]
	v_pk_fma_f32 v[108:109], v[108:109], v[132:133], v[188:189]
	v_pk_fma_f32 v[106:107], v[106:107], v[130:131], v[186:187]
	global_store_dwordx4 v[226:227], v[126:129], off sc0 sc1
	global_store_dwordx4 v[226:227], v[122:125], off offset:64 sc0 sc1
	global_store_dwordx4 v[226:227], v[118:121], off offset:512 sc0 sc1
	global_store_dwordx4 v[226:227], v[106:109], off offset:576 sc0 sc1
	v_lshl_add_u64 v[250:251], v[154:155], 0, v[168:169]
	v_lshlrev_b64 v[250:251], 2, v[250:251]
	v_lshl_add_u64 v[218:219], s[0:1], 0, v[250:251]
	global_load_dwordx4 v[174:177], v[218:219], off
	global_load_dwordx4 v[178:181], v[218:219], off offset:64
	global_load_dwordx4 v[182:185], v[218:219], off offset:512
	global_load_dwordx4 v[186:189], v[218:219], off offset:576
	s_waitcnt vmcnt(12)
	v_lshl_add_u64 v[250:251], v[150:151], 0, v[168:169]
	v_lshlrev_b64 v[250:251], 2, v[250:251]
	v_lshl_add_u64 v[226:227], s[50:51], 0, v[250:251]
	v_pk_fma_f32 v[116:117], v[116:117], v[144:145], v[192:193]
	v_pk_fma_f32 v[114:115], v[114:115], v[142:143], v[190:191]
	v_pk_fma_f32 v[112:113], v[112:113], v[140:141], v[196:197]
	v_pk_fma_f32 v[110:111], v[110:111], v[138:139], v[194:195]
	v_pk_fma_f32 v[104:105], v[104:105], v[136:137], v[200:201]
	v_pk_fma_f32 v[102:103], v[102:103], v[134:135], v[198:199]
	v_pk_fma_f32 v[92:93], v[92:93], v[132:133], v[204:205]
	v_pk_fma_f32 v[90:91], v[90:91], v[130:131], v[202:203]
	global_store_dwordx4 v[226:227], v[114:117], off sc0 sc1
	global_store_dwordx4 v[226:227], v[110:113], off offset:64 sc0 sc1
	global_store_dwordx4 v[226:227], v[102:105], off offset:512 sc0 sc1
	global_store_dwordx4 v[226:227], v[90:93], off offset:576 sc0 sc1
	v_lshl_add_u64 v[250:251], v[156:157], 0, v[168:169]
	v_lshlrev_b64 v[250:251], 2, v[250:251]
	v_lshl_add_u64 v[218:219], s[0:1], 0, v[250:251]
	global_load_dwordx4 v[190:193], v[218:219], off
	global_load_dwordx4 v[194:197], v[218:219], off offset:64
	global_load_dwordx4 v[198:201], v[218:219], off offset:512
	global_load_dwordx4 v[202:205], v[218:219], off offset:576
	s_waitcnt vmcnt(16)
	v_lshl_add_u64 v[250:251], v[152:153], 0, v[168:169]
	v_lshlrev_b64 v[250:251], 2, v[250:251]
	v_lshl_add_u64 v[226:227], s[50:51], 0, v[250:251]
	v_pk_fma_f32 v[100:101], v[100:101], v[144:145], v[236:237]
	v_pk_fma_f32 v[98:99], v[98:99], v[142:143], v[234:235]
	v_pk_fma_f32 v[96:97], v[96:97], v[140:141], v[240:241]
	v_pk_fma_f32 v[94:95], v[94:95], v[138:139], v[238:239]
	v_pk_fma_f32 v[88:89], v[88:89], v[136:137], v[244:245]
	v_pk_fma_f32 v[86:87], v[86:87], v[134:135], v[242:243]
	v_pk_fma_f32 v[76:77], v[76:77], v[132:133], v[248:249]
	v_pk_fma_f32 v[74:75], v[74:75], v[130:131], v[246:247]
	global_store_dwordx4 v[226:227], v[98:101], off sc0 sc1
	global_store_dwordx4 v[226:227], v[94:97], off offset:64 sc0 sc1
	global_store_dwordx4 v[226:227], v[86:89], off offset:512 sc0 sc1
	global_store_dwordx4 v[226:227], v[74:77], off offset:576 sc0 sc1
	v_lshl_add_u64 v[250:251], v[158:159], 0, v[168:169]
	v_lshlrev_b64 v[250:251], 2, v[250:251]
	v_lshl_add_u64 v[218:219], s[0:1], 0, v[250:251]
	global_load_dwordx4 v[234:237], v[218:219], off
	global_load_dwordx4 v[238:241], v[218:219], off offset:64
	global_load_dwordx4 v[242:245], v[218:219], off offset:512
	global_load_dwordx4 v[246:249], v[218:219], off offset:576
	s_waitcnt vmcnt(16)
	v_lshl_add_u64 v[250:251], v[154:155], 0, v[168:169]
	v_lshlrev_b64 v[250:251], 2, v[250:251]
	v_lshl_add_u64 v[226:227], s[50:51], 0, v[250:251]
	v_pk_fma_f32 v[84:85], v[84:85], v[144:145], v[176:177]
	v_pk_fma_f32 v[82:83], v[82:83], v[142:143], v[174:175]
	v_pk_fma_f32 v[80:81], v[80:81], v[140:141], v[180:181]
	v_pk_fma_f32 v[78:79], v[78:79], v[138:139], v[178:179]
	v_pk_fma_f32 v[72:73], v[72:73], v[136:137], v[184:185]
	v_pk_fma_f32 v[70:71], v[70:71], v[134:135], v[182:183]
	v_pk_fma_f32 v[68:69], v[68:69], v[132:133], v[188:189]
	v_pk_fma_f32 v[66:67], v[66:67], v[130:131], v[186:187]
	global_store_dwordx4 v[226:227], v[82:85], off sc0 sc1
	global_store_dwordx4 v[226:227], v[78:81], off offset:64 sc0 sc1
	global_store_dwordx4 v[226:227], v[70:73], off offset:512 sc0 sc1
	global_store_dwordx4 v[226:227], v[66:69], off offset:576 sc0 sc1
	v_lshl_add_u64 v[250:251], v[160:161], 0, v[168:169]
	v_lshlrev_b64 v[250:251], 2, v[250:251]
	v_lshl_add_u64 v[218:219], s[0:1], 0, v[250:251]
	global_load_dwordx4 v[174:177], v[218:219], off
	global_load_dwordx4 v[178:181], v[218:219], off offset:64
	global_load_dwordx4 v[182:185], v[218:219], off offset:512
	global_load_dwordx4 v[186:189], v[218:219], off offset:576
	s_waitcnt vmcnt(16)
	v_lshl_add_u64 v[250:251], v[156:157], 0, v[168:169]
	v_lshlrev_b64 v[250:251], 2, v[250:251]
	v_lshl_add_u64 v[226:227], s[50:51], 0, v[250:251]
	v_pk_fma_f32 v[64:65], v[64:65], v[144:145], v[192:193]
	v_pk_fma_f32 v[62:63], v[62:63], v[142:143], v[190:191]
	v_pk_fma_f32 v[60:61], v[60:61], v[140:141], v[196:197]
	v_pk_fma_f32 v[58:59], v[58:59], v[138:139], v[194:195]
	v_pk_fma_f32 v[56:57], v[56:57], v[136:137], v[200:201]
	v_pk_fma_f32 v[54:55], v[54:55], v[134:135], v[198:199]
	v_pk_fma_f32 v[44:45], v[44:45], v[132:133], v[204:205]
	v_pk_fma_f32 v[42:43], v[42:43], v[130:131], v[202:203]
	global_store_dwordx4 v[226:227], v[62:65], off sc0 sc1
	global_store_dwordx4 v[226:227], v[58:61], off offset:64 sc0 sc1
	global_store_dwordx4 v[226:227], v[54:57], off offset:512 sc0 sc1
	global_store_dwordx4 v[226:227], v[42:45], off offset:576 sc0 sc1
	v_lshl_add_u64 v[250:251], v[162:163], 0, v[168:169]
	v_lshlrev_b64 v[250:251], 2, v[250:251]
	v_lshl_add_u64 v[218:219], s[0:1], 0, v[250:251]
	global_load_dwordx4 v[190:193], v[218:219], off
	global_load_dwordx4 v[194:197], v[218:219], off offset:64
	global_load_dwordx4 v[198:201], v[218:219], off offset:512
	global_load_dwordx4 v[202:205], v[218:219], off offset:576
	s_waitcnt vmcnt(16)
	v_lshl_add_u64 v[250:251], v[158:159], 0, v[168:169]
	v_lshlrev_b64 v[250:251], 2, v[250:251]
	v_lshl_add_u64 v[226:227], s[50:51], 0, v[250:251]
	v_pk_fma_f32 v[52:53], v[52:53], v[144:145], v[236:237]
	v_pk_fma_f32 v[50:51], v[50:51], v[142:143], v[234:235]
	v_pk_fma_f32 v[48:49], v[48:49], v[140:141], v[240:241]
	v_pk_fma_f32 v[46:47], v[46:47], v[138:139], v[238:239]
	v_pk_fma_f32 v[40:41], v[40:41], v[136:137], v[244:245]
	v_pk_fma_f32 v[38:39], v[38:39], v[134:135], v[242:243]
	v_pk_fma_f32 v[28:29], v[28:29], v[132:133], v[248:249]
	v_pk_fma_f32 v[26:27], v[26:27], v[130:131], v[246:247]
	global_store_dwordx4 v[226:227], v[50:53], off sc0 sc1
	global_store_dwordx4 v[226:227], v[46:49], off offset:64 sc0 sc1
	global_store_dwordx4 v[226:227], v[38:41], off offset:512 sc0 sc1
	global_store_dwordx4 v[226:227], v[26:29], off offset:576 sc0 sc1
	s_waitcnt vmcnt(12)
	v_lshl_add_u64 v[250:251], v[160:161], 0, v[168:169]
	v_lshlrev_b64 v[250:251], 2, v[250:251]
	v_lshl_add_u64 v[226:227], s[50:51], 0, v[250:251]
	v_pk_fma_f32 v[36:37], v[36:37], v[144:145], v[176:177]
	v_pk_fma_f32 v[34:35], v[34:35], v[142:143], v[174:175]
	v_pk_fma_f32 v[32:33], v[32:33], v[140:141], v[180:181]
	v_pk_fma_f32 v[30:31], v[30:31], v[138:139], v[178:179]
	v_pk_fma_f32 v[24:25], v[24:25], v[136:137], v[184:185]
	v_pk_fma_f32 v[22:23], v[22:23], v[134:135], v[182:183]
	v_pk_fma_f32 v[12:13], v[12:13], v[132:133], v[188:189]
	v_pk_fma_f32 v[10:11], v[10:11], v[130:131], v[186:187]
	global_store_dwordx4 v[226:227], v[34:37], off sc0 sc1
	global_store_dwordx4 v[226:227], v[30:33], off offset:64 sc0 sc1
	global_store_dwordx4 v[226:227], v[22:25], off offset:512 sc0 sc1
	global_store_dwordx4 v[226:227], v[10:13], off offset:576 sc0 sc1
	s_waitcnt vmcnt(8)
	v_lshl_add_u64 v[250:251], v[162:163], 0, v[168:169]
	v_lshlrev_b64 v[250:251], 2, v[250:251]
	v_lshl_add_u64 v[226:227], s[50:51], 0, v[250:251]
	v_pk_fma_f32 v[20:21], v[20:21], v[144:145], v[192:193]
	v_pk_fma_f32 v[18:19], v[18:19], v[142:143], v[190:191]
	v_pk_fma_f32 v[16:17], v[16:17], v[140:141], v[196:197]
	v_pk_fma_f32 v[14:15], v[14:15], v[138:139], v[194:195]
	v_pk_fma_f32 v[8:9], v[8:9], v[136:137], v[200:201]
	v_pk_fma_f32 v[6:7], v[6:7], v[134:135], v[198:199]
	v_pk_fma_f32 v[4:5], v[4:5], v[132:133], v[204:205]
	v_pk_fma_f32 v[2:3], v[2:3], v[130:131], v[202:203]
	global_store_dwordx4 v[226:227], v[18:21], off sc0 sc1
	global_store_dwordx4 v[226:227], v[14:17], off offset:64 sc0 sc1
	global_store_dwordx4 v[226:227], v[6:9], off offset:512 sc0 sc1
	global_store_dwordx4 v[226:227], v[2:5], off offset:576 sc0 sc1
	s_mov_b64 s[50:51], s[86:87]
	v_readlane_b32 s86, v255, 33
	v_readlane_b32 s87, v255, 34
	s_cbranch_vccnz .LBB0_486
